# one static s_setprio 1 for waves 0-3 at kernel entry (mirror of the previous)
# speedup vs baseline: 1.0014x; 1.0014x over previous
; #define LAS __attribute__((address_space(3)))
; __global__ void __launch_bounds__(NTHR, 2) fwd_kernel(Params P) {
;     extern __shared__ __attribute__((aligned(16))) unsigned char lds[];
;     const int bid = blockIdx.x, nb = gridDim.x;
;     unsigned char* sm = lds + 16;
;     ...
;     if (threadIdx.x == 0) { ((volatile unsigned*)lds)[0] = 0u; ((volatile unsigned*)lds)[1] = 0u; ((volatile unsigned*)lds)[2] = 0u; ((volatile unsigned*)lds)[3] = 0u; }
;     __syncthreads();
;     XcdBarrier bar = xcd_barrier_post((unsigned*)P.ws, (volatile LAS unsigned*)lds);
_Z10fwd_kernel6Params:
	s_load_dwordx8 s[4:11], s[0:1], 0x140
	s_mov_b32 s44, s2
	v_readfirstlane_b32 s96, v0
	s_nop 3
	s_lshr_b32 s96, s96, 6
	s_cmp_ge_u32 s96, 4
	s_cbranch_scc1 .Lprio_done
	s_setprio 1
